# b1_bundle
# speedup vs baseline: 1.0022x; 1.0022x over previous
_Z10attn64_fwdPKDF16_S0_S0_PDF16_:
	s_load_dwordx8 s[4:11], s[0:1], 0x0
	s_lshr_b32 s0, s2, 3
	s_and_b32 s42, s2, 7
	s_bfe_u32 s1, s2, 0x30003
	s_and_b32 s0, s0, 8
	s_bfe_u32 s14, s2, 0x10007
	s_or_b32 s19, s0, s42
	s_xor_b32 s0, s1, 15
	s_cmpk_lt_u32 s2, 0x100
	s_cselect_b32 s18, s0, s1
	v_readfirstlane_b32 s3, v0
	s_lshr_b32 s33, s3, 6
	s_lshl_b32 s0, s14, 11
	s_lshl_b32 s43, s18, 7
	s_or_b32 s0, s43, s0
	s_lshl_b32 s21, s33, 5
	s_add_i32 s12, s0, s21
	s_mov_b32 s13, 0
	s_lshl_b64 s[0:1], s[12:13], 11
	s_waitcnt lgkmcnt(0)
	s_add_u32 s0, s4, s0
	s_addc_u32 s1, s5, s1
	s_lshl_b32 s15, s19, 7
	s_add_u32 s0, s0, s15
	s_addc_u32 s1, s1, 0
	s_lshl_b32 s14, s14, 22
	s_add_u32 s4, s6, s14
	s_addc_u32 s5, s7, 0
	v_and_b32_e32 v236, 63, v0
	s_add_u32 s4, s4, s15
	s_addc_u32 s5, s5, 0
	v_lshlrev_b32_e32 v200, 11, v236
	v_mov_b32_e32 v201, 0
	v_lshl_add_u64 v[2:3], s[4:5], 0, v[200:201]
	s_lshl_b32 s4, s33, 4
	s_mov_b32 s5, s13
	v_lshl_add_u64 v[34:35], v[2:3], 0, s[4:5]
	s_add_u32 s5, s8, s14
	s_addc_u32 s16, s9, 0
	s_add_u32 s14, s5, s15
	v_bfe_u32 v1, v0, 2, 4
	s_addc_u32 s15, s16, 0
	v_or_b32_e32 v2, s4, v1
	v_mov_b32_e32 v3, v201
	s_lshl_b32 s5, s33, 10
	v_lshlrev_b64 v[2:3], 11, v[2:3]
	v_lshlrev_b32_e32 v237, 3, v0
	s_cmp_lg_u32 0, -1
	v_lshl_add_u64 v[2:3], s[14:15], 0, v[2:3]
	v_and_b32_e32 v38, 24, v237
	s_cselect_b32 s14, 0, 0
	v_lshlrev_b32_e32 v4, 1, v38
	v_mov_b32_e32 v5, v201
	s_add_i32 s38, s5, s14
	s_mov_b32 s14, m0
	s_mov_b32 m0, s38
	s_nop 0
	global_load_lds_dwordx4 v[34:35], off
	s_mov_b32 m0, s14
	v_lshl_add_u64 v[36:37], v[2:3], 0, v[4:5]
	v_lshl_add_u64 v[2:3], v[34:35], 0, 64
	s_add_i32 s20, s38, 0x1000
	s_mov_b32 s14, m0
	s_mov_b32 m0, s20
	s_nop 0
	global_load_lds_dwordx4 v[2:3], off
	s_mov_b32 m0, s14
	s_add_i32 s39, s38, 0x6000
	s_mov_b32 s14, m0
	s_mov_b32 m0, s39
	s_nop 0
	global_load_lds_dwordx4 v[36:37], off
	s_mov_b32 m0, s14
	v_lshl_add_u64 v[2:3], v[36:37], 0, 64
	s_add_i32 s14, s38, 0x7000
	s_mov_b32 s15, m0
	s_mov_b32 m0, s14
	s_nop 0
	global_load_lds_dwordx4 v[2:3], off
	s_mov_b32 m0, s15
	s_mov_b64 s[14:15], 0x20000
	v_lshl_add_u64 v[2:3], v[34:35], 0, s[14:15]
	s_add_i32 s14, s38, 0x2000
	s_mov_b32 s15, m0
	s_mov_b32 m0, s14
	s_nop 0
	global_load_lds_dwordx4 v[2:3], off
	s_mov_b32 m0, s15
	s_mov_b64 s[14:15], 0x20040
	v_and_b32_e32 v238, 31, v0
	v_lshl_add_u64 v[2:3], v[34:35], 0, s[14:15]
	v_bfe_u32 v212, v0, 5, 1
	s_add_i32 s14, s38, 0x3000
	s_mov_b32 s15, m0
	s_mov_b32 m0, s14
	s_nop 0
	global_load_lds_dwordx4 v[2:3], off
	s_mov_b32 m0, s15
	s_mov_b64 s[14:15], 0x20000
	v_lshl_add_u64 v[2:3], v[36:37], 0, s[14:15]
	s_add_i32 s14, s38, 0x8000
	s_mov_b32 s15, m0
	s_mov_b32 m0, s14
	s_nop 0
	global_load_lds_dwordx4 v[2:3], off
	s_mov_b32 m0, s15
	s_mov_b64 s[14:15], 0x20040
	v_lshl_add_u64 v[2:3], v[36:37], 0, s[14:15]
	s_add_i32 s14, s38, 0x9000
	s_mov_b32 s15, m0
	s_mov_b32 m0, s14
	s_nop 0
	global_load_lds_dwordx4 v[2:3], off
	s_mov_b32 m0, s15
	v_lshlrev_b32_e32 v2, 11, v238
	v_lshl_or_b32 v2, v212, 4, v2
	global_load_dwordx4 v[148:151], v2, s[0:1]
	global_load_dwordx4 v[140:143], v2, s[0:1] offset:32
	global_load_dwordx4 v[136:139], v2, s[0:1] offset:64
	global_load_dwordx4 v[132:135], v2, s[0:1] offset:96
	s_cmp_eq_u32 s18, 0
	v_mov_b32_e32 v128, 0x3c003c00
	s_cselect_b64 s[0:1], -1, 0
	s_cmp_lg_u32 s18, 0
	v_mov_b32_e32 v129, v128
	v_mov_b32_e32 v130, v128
	v_mov_b32_e32 v131, v128
	s_cselect_b64 s[14:15], -1, 0
	s_mov_b64 s[16:17], -1
	s_and_b64 vcc, exec, s[0:1]
	s_cbranch_vccnz .LBB1_2
	s_mov_b64 s[16:17], 0x40000
	s_cmp_lg_u32 0, -1
	v_lshl_add_u64 v[2:3], v[34:35], 0, s[16:17]
	s_cselect_b32 s16, 0, 0
	s_add_i32 s22, s16, s5
	s_add_i32 s16, s22, 0x4000
	s_mov_b32 s17, m0
	s_mov_b32 m0, s16
	s_nop 0
	global_load_lds_dwordx4 v[2:3], off
	s_mov_b32 m0, s17
	s_mov_b64 s[16:17], 0x40040
	v_lshl_add_u64 v[2:3], v[34:35], 0, s[16:17]
	s_addk_i32 s22, 0x5000
	s_mov_b32 s16, m0
	s_mov_b32 m0, s22
	s_nop 0
	global_load_lds_dwordx4 v[2:3], off
	s_mov_b32 m0, s16
	s_waitcnt vmcnt(6) lgkmcnt(0)
	s_barrier
	s_mov_b64 s[16:17], 0

.LBB1_8:
	ds_read_b128 v[192:195], v243 offset:8192
	ds_read_b128 v[188:191], v243 offset:8704
	ds_read_b128 v[184:187], v243 offset:10240
	ds_read_b128 v[176:179], v243 offset:10752
	ds_read_b128 v[180:183], v243 offset:12288
	ds_read_b128 v[172:175], v243 offset:12800
	ds_read_b128 v[168:171], v243 offset:14336
	ds_read_b128 v[164:167], v243 offset:14848
	s_and_b64 vcc, exec, s[0:1]
	s_mov_b64 s[0:1], -1
	s_cbranch_vccnz .LBB1_10
	s_waitcnt vmcnt(4) lgkmcnt(0)
	s_barrier
	s_mov_b64 s[0:1], 0

.Lg1_cloop:
	s_lshl_b32 s12, s8, 14
	v_add3_u32 v42, s12, v37, v35
	v_add3_u32 v58, s12, v36, v35
	s_waitcnt vmcnt(3)
	s_barrier
	ds_read_b128 v[38:41], v42 offset:8192
	ds_read_b128 v[42:45], v42 offset:9216
	ds_read_b128 v[46:49], v58
	ds_read_b128 v[50:53], v58 offset:1024
	ds_read_b128 v[54:57], v58 offset:2048
	ds_read_b128 v[58:61], v58 offset:3072
	s_lshl_b32 s13, s17, 14
	s_add_i32 m0, s13, s16
	s_add_i32 s13, s17, 1
	global_load_lds_dwordx4 v62, s[14:15]
	s_cmp_lg_u32 s17, 4
	s_cselect_b32 s17, s13, 0
	v_add_u32_e32 v62, 64, v62
	s_waitcnt lgkmcnt(0)
	v_mfma_f32_16x16x32_f16 v[30:33], v[46:49], v[38:41], v[30:33]
	s_add_i32 s12, s8, 1
	s_cmp_lg_u32 s8, 4
	s_cselect_b32 s8, s12, 0
	v_mfma_f32_16x16x32_f16 v[22:25], v[46:49], v[42:45], v[22:25]
	s_add_i32 s11, s11, -1
	s_cmp_eq_u32 s11, 0
	v_mfma_f32_16x16x32_f16 v[26:29], v[50:53], v[38:41], v[26:29]
	v_mfma_f32_16x16x32_f16 v[14:17], v[50:53], v[42:45], v[14:17]
	v_mfma_f32_16x16x32_f16 v[18:21], v[54:57], v[38:41], v[18:21]
	v_mfma_f32_16x16x32_f16 v[6:9], v[54:57], v[42:45], v[6:9]
	v_mfma_f32_16x16x32_f16 v[10:13], v[58:61], v[38:41], v[10:13]
	v_mfma_f32_16x16x32_f16 v[2:5], v[58:61], v[42:45], v[2:5]
	s_cbranch_scc0 .Lg1_cloop
	s_mul_i32 s12, s6, 8704
	s_add_i32 s12, s12, 0x14000
	v_mul_u32_u24_e32 v35, 272, v34
	v_lshl_add_u32 v35, v1, 4, v35
	v_add_u32_e32 v35, s12, v35
	v_mul_u32_u24_e32 v36, 272, v1
	v_lshl_add_u32 v36, v34, 4, v36
	v_add_u32_e32 v36, s12, v36
	v_lshlrev_b32_e32 v37, 12, v1
	v_lshl_add_u32 v37, v34, 4, v37
	s_add_i32 s8, s10, s4
	s_lshl_b32 s8, s8, 12
	s_add_i32 s11, s7, s9
	s_lshl_b32 s11, s11, 2
	s_add_i32 s8, s8, s11
	s_add_u32 s2, s2, s8
	s_addc_u32 s3, s3, 0
	ds_write_b128 v35, v[30:33] offset:0
	ds_write_b128 v35, v[22:25] offset:4352
	ds_write_b128 v35, v[26:29] offset:64
	ds_write_b128 v35, v[14:17] offset:4416
	ds_write_b128 v35, v[18:21] offset:128
	ds_write_b128 v35, v[6:9] offset:4480
	ds_write_b128 v35, v[10:13] offset:192
	ds_write_b128 v35, v[2:5] offset:4544
	s_waitcnt lgkmcnt(0)
	ds_read_b128 v[2:5], v36 offset:0
	ds_read_b128 v[6:9], v36 offset:1088
	ds_read_b128 v[10:13], v36 offset:2176
	ds_read_b128 v[14:17], v36 offset:3264
	ds_read_b128 v[18:21], v36 offset:4352
	ds_read_b128 v[22:25], v36 offset:5440
	ds_read_b128 v[26:29], v36 offset:6528
	ds_read_b128 v[30:33], v36 offset:7616
	s_waitcnt lgkmcnt(7)
	global_store_dwordx4 v37, v[2:5], s[2:3] sc1
	v_add_u32_e32 v37, 0x4000, v37
	s_waitcnt lgkmcnt(6)
	global_store_dwordx4 v37, v[6:9], s[2:3] sc1
	v_add_u32_e32 v37, 0x4000, v37
	s_waitcnt lgkmcnt(5)
	global_store_dwordx4 v37, v[10:13], s[2:3] sc1
	v_add_u32_e32 v37, 0x4000, v37
	s_waitcnt lgkmcnt(4)
	global_store_dwordx4 v37, v[14:17], s[2:3] sc1
	v_add_u32_e32 v37, 0x4000, v37
	s_waitcnt lgkmcnt(3)
	global_store_dwordx4 v37, v[18:21], s[2:3] sc1
	v_add_u32_e32 v37, 0x4000, v37
	s_waitcnt lgkmcnt(2)
	global_store_dwordx4 v37, v[22:25], s[2:3] sc1
	v_add_u32_e32 v37, 0x4000, v37
	s_waitcnt lgkmcnt(1)
	global_store_dwordx4 v37, v[26:29], s[2:3] sc1
	v_add_u32_e32 v37, 0x4000, v37
	s_waitcnt lgkmcnt(0)
	global_store_dwordx4 v37, v[30:33], s[2:3] sc1
	v_add_u32_e32 v37, 0x4000, v37
	s_branch .LBB3_2

	.amdhsa_kernel _Z11gemm_kernelILi1ELi4ELi2ELi5EEvPKDF16_S1_PK15HIP_vector_typeIfLj4EEPDF16_S6_S6_Pf
		.amdhsa_group_segment_fixed_size 69632
		.amdhsa_private_segment_fixed_size 0
		.amdhsa_kernarg_size 56
		.amdhsa_user_sgpr_count 2
		.amdhsa_user_sgpr_dispatch_ptr 0
		.amdhsa_user_sgpr_queue_ptr 0
		.amdhsa_user_sgpr_kernarg_segment_ptr 1
		.amdhsa_user_sgpr_dispatch_id 0
		.amdhsa_user_sgpr_kernarg_preload_length 0
		.amdhsa_user_sgpr_kernarg_preload_offset 0
		.amdhsa_user_sgpr_private_segment_size 0
		.amdhsa_uses_dynamic_stack 0
		.amdhsa_enable_private_segment 0
		.amdhsa_system_sgpr_workgroup_id_x 1
		.amdhsa_system_sgpr_workgroup_id_y 0
		.amdhsa_system_sgpr_workgroup_id_z 0
		.amdhsa_system_sgpr_workgroup_info 0
		.amdhsa_system_vgpr_workitem_id 0
		.amdhsa_next_free_vgpr 66
		.amdhsa_next_free_sgpr 32
		.amdhsa_accum_offset 68
		.amdhsa_reserve_vcc 1
		.amdhsa_float_round_mode_32 0
		.amdhsa_float_round_mode_16_64 0
		.amdhsa_float_denorm_mode_32 3
		.amdhsa_float_denorm_mode_16_64 3
		.amdhsa_dx10_clamp 1
		.amdhsa_ieee_mode 1
		.amdhsa_fp16_overflow 0
		.amdhsa_tg_split 0
		.amdhsa_exception_fp_ieee_invalid_op 0
		.amdhsa_exception_fp_denorm_src 0
		.amdhsa_exception_fp_ieee_div_zero 0
		.amdhsa_exception_fp_ieee_overflow 0
		.amdhsa_exception_fp_ieee_underflow 0
		.amdhsa_exception_fp_ieee_inexact 0
		.amdhsa_exception_int_div_zero 0
	.end_amdhsa_kernel

amdhsa.kernels:
  - .agpr_count:     0
    .args:
      - .address_space:  global
        .offset:         0
        .size:           8
        .value_kind:     global_buffer
      - .address_space:  global
        .offset:         8
        .size:           8
        .value_kind:     global_buffer
      - .address_space:  global
        .offset:         16
        .size:           8
        .value_kind:     global_buffer
      - .address_space:  global
        .offset:         24
        .size:           8
        .value_kind:     global_buffer
      - .address_space:  global
        .offset:         32
        .size:           8
        .value_kind:     global_buffer
      - .actual_access:  write_only
        .address_space:  global
        .offset:         40
        .size:           8
        .value_kind:     global_buffer
      - .actual_access:  write_only
        .address_space:  global
        .offset:         48
        .size:           8
        .value_kind:     global_buffer
      - .actual_access:  write_only
        .address_space:  global
        .offset:         56
        .size:           8
        .value_kind:     global_buffer
      - .actual_access:  write_only
        .address_space:  global
        .offset:         64
        .size:           8
        .value_kind:     global_buffer
    .group_segment_fixed_size: 0
    .kernarg_segment_align: 8
    .kernarg_segment_size: 72
    .language:       OpenCL C
    .language_version:
      - 2
      - 0
    .max_flat_workgroup_size: 256
    .name:           _Z11prep_kernelPKfS0_S0_S0_S0_PDF16_S1_S1_P15HIP_vector_typeIfLj2EE
    .private_segment_fixed_size: 0
    .sgpr_count:     38
    .sgpr_spill_count: 0
    .symbol:         _Z11prep_kernelPKfS0_S0_S0_S0_PDF16_S1_S1_P15HIP_vector_typeIfLj2EE.kd
    .uniform_work_group_size: 1
    .uses_dynamic_stack: false
    .vgpr_count:     44
    .vgpr_spill_count: 0
    .wavefront_size: 64
  - .agpr_count:     0
    .args:
      - .address_space:  global
        .offset:         0
        .size:           8
        .value_kind:     global_buffer
      - .address_space:  global
        .offset:         8
        .size:           8
        .value_kind:     global_buffer
      - .address_space:  global
        .offset:         16
        .size:           8
        .value_kind:     global_buffer
      - .address_space:  global
        .offset:         24
        .size:           8
        .value_kind:     global_buffer
    .group_segment_fixed_size: 0
    .kernarg_segment_align: 8
    .kernarg_segment_size: 32
    .language:       OpenCL C
    .language_version:
      - 2
      - 0
    .max_flat_workgroup_size: 256
    .name:           _Z10attn64_fwdPKDF16_S0_S0_PDF16_
    .private_segment_fixed_size: 0
    .sgpr_count:     55
    .sgpr_spill_count: 0
    .symbol:         _Z10attn64_fwdPKDF16_S0_S0_PDF16_.kd
    .uniform_work_group_size: 1
    .uses_dynamic_stack: false
    .vgpr_count:     248
    .vgpr_spill_count: 0
    .wavefront_size: 64
  - .agpr_count:     0
    .args:
      - .address_space:  global
        .offset:         0
        .size:           8
        .value_kind:     global_buffer
      - .address_space:  global
        .offset:         8
        .size:           8
        .value_kind:     global_buffer
      - .actual_access:  read_only
        .address_space:  global
        .offset:         16
        .size:           8
        .value_kind:     global_buffer
      - .actual_access:  write_only
        .address_space:  global
        .offset:         24
        .size:           8
        .value_kind:     global_buffer
      - .actual_access:  write_only
        .address_space:  global
        .offset:         32
        .size:           8
        .value_kind:     global_buffer
      - .actual_access:  write_only
        .address_space:  global
        .offset:         40
        .size:           8
        .value_kind:     global_buffer
      - .actual_access:  read_only
        .address_space:  global
        .offset:         48
        .size:           8
        .value_kind:     global_buffer
    .group_segment_fixed_size: 0
    .kernarg_segment_align: 8
    .kernarg_segment_size: 56
    .language:       OpenCL C
    .language_version:
      - 2
      - 0
    .max_flat_workgroup_size: 768
    .name:           _Z11gemm_kernelILi0ELi6ELi4ELi5EEvPKDF16_S1_PK15HIP_vector_typeIfLj4EEPDF16_S6_S6_Pf
    .private_segment_fixed_size: 0
    .sgpr_count:     56
    .sgpr_spill_count: 0
    .symbol:         _Z11gemm_kernelILi0ELi6ELi4ELi5EEvPKDF16_S1_PK15HIP_vector_typeIfLj4EEPDF16_S6_S6_Pf.kd
    .uniform_work_group_size: 1
    .uses_dynamic_stack: false
    .vgpr_count:     168
    .vgpr_spill_count: 0
    .wavefront_size: 64
  - .agpr_count:     0
    .args:
      - .address_space:  global
        .offset:         0
        .size:           8
        .value_kind:     global_buffer
      - .address_space:  global
        .offset:         8
        .size:           8
        .value_kind:     global_buffer
      - .actual_access:  read_only
        .address_space:  global
        .offset:         16
        .size:           8
        .value_kind:     global_buffer
      - .actual_access:  read_only
        .address_space:  global
        .offset:         24
        .size:           8
        .value_kind:     global_buffer
      - .actual_access:  read_only
        .address_space:  global
        .offset:         32
        .size:           8
        .value_kind:     global_buffer
      - .actual_access:  read_only
        .address_space:  global
        .offset:         40
        .size:           8
        .value_kind:     global_buffer
      - .actual_access:  write_only
        .address_space:  global
        .offset:         48
        .size:           8
        .value_kind:     global_buffer
    .group_segment_fixed_size: 69632
    .kernarg_segment_align: 8
    .kernarg_segment_size: 56
    .language:       OpenCL C
    .language_version:
      - 2
      - 0
    .max_flat_workgroup_size: 768
    .name:           _Z11gemm_kernelILi1ELi4ELi2ELi5EEvPKDF16_S1_PK15HIP_vector_typeIfLj4EEPDF16_S6_S6_Pf
    .private_segment_fixed_size: 0
    .sgpr_count:     38
    .sgpr_spill_count: 0
    .symbol:         _Z11gemm_kernelILi1ELi4ELi2ELi5EEvPKDF16_S1_PK15HIP_vector_typeIfLj4EEPDF16_S6_S6_Pf.kd
    .uniform_work_group_size: 1
    .uses_dynamic_stack: false
    .vgpr_count:     66
    .vgpr_spill_count: 0
    .wavefront_size: 64
